# router expert counters moved to separate cache lines (ws+0x10000+e*0x1100): atomics no longer serialize on one line
# speedup vs baseline: 1.0668x; 1.0668x over previous
; #define LAS __attribute__((address_space(3)))
; __device__ __forceinline__ float bflo(unsigned w) { return __uint_as_float(w << 16); }
; __device__ __forceinline__ float bfhi(unsigned w) { return __uint_as_float(w & 0xffff0000u); }
; template <bool ROUTER, bool OUT8, bool IN16>
; __device__ __forceinline__ void rms_rows(const Ctx& X, const void* __restrict__ Xin, void* __restrict__ Hv, const LAS float* sh, const LAS float* gs,
;                                          const LAS float* router_w_lds, unsigned* cnt, unsigned* route) {
;     ...
;     for (int t = X.gw; t < NTOK; t += X.ngw) {
;         f32x4 v[8]; float s = 0.f;
; #pragma unroll
;         for (int j = 0; j < 8; ++j) { if (IN16) v[j] = (f32x4){bflo(nr[j].x), bfhi(nr[j].x), bflo(nr[j].y), bfhi(nr[j].y)}; else v[j] = nv[j]; }
;         if (t + X.ngw < NTOK) {
;             if (IN16) { const v2u* xr = (const v2u*)((const bf16*)Xin + (size_t)(t + X.ngw) * DM) + X.lane;
; #pragma unroll
;                 for (int j = 0; j < 8; ++j) nr[j] = xr[64 * j]; }
;             else { const f32x4* xr = (const f32x4*)((const float*)Xin + (size_t)(t + X.ngw) * DM) + X.lane;
; #pragma unroll
;                 for (int j = 0; j < 8; ++j) nv[j] = xr[64 * j]; } }
;         asm volatile("" ::: "memory");
; #pragma unroll
;         for (int j = 0; j < 8; ++j) s += (v[j][0] * v[j][0] + v[j][1] * v[j][1]) + (v[j][2] * v[j][2] + v[j][3] * v[j][3]);
;         s = wave_sum(s);
;         const float r = 1.0f / sqrtf(s * (1.0f / DM) + EPSF);
;         float lg[8]; unsigned hq[8];
;         if (ROUTER) {
; #pragma unroll
;             for (int e = 0; e < 8; ++e) lg[e] = 0.f; }
; #pragma unroll
;         for (int j = 0; j < 8; ++j) { const int c = 4 * X.lane + 256 * j;
;             const f32x4 g4 = *(const LAS f32x4*)(gs + c), s4 = *(const LAS f32x4*)(sh + c);
;             const f32x4 h = v[j] * r * g4 + s4;
.LBB0_3571:
	v_and_b32_e32 v23, 0xffff0000, v9
	v_lshlrev_b32_e32 v20, 16, v8
	v_and_b32_e32 v21, 0xffff0000, v8
	v_lshlrev_b32_e32 v22, 16, v9
	v_lshlrev_b32_e32 v33, 16, v7
	v_lshlrev_b32_e32 v32, 16, v6
	v_and_b32_e32 v61, 0xffff0000, v7
	v_and_b32_e32 v60, 0xffff0000, v6
	v_lshlrev_b32_e32 v6, 16, v4
	v_and_b32_e32 v7, 0xffff0000, v4
	v_lshlrev_b32_e32 v8, 16, v5
	v_and_b32_e32 v9, 0xffff0000, v5
	v_and_b32_e32 v5, 0xffff0000, v2
	v_mul_f32_e32 v4, v23, v23
	v_lshlrev_b32_e32 v79, 16, v12
	v_and_b32_e32 v77, 0xffff0000, v12
	v_lshlrev_b32_e32 v74, 16, v13
	v_and_b32_e32 v75, 0xffff0000, v13
	v_pk_fma_f32 v[12:13], v[22:23], v[22:23], v[4:5] op_sel_hi:[1,1,0]
	v_mul_f32_e32 v4, v21, v21
	v_lshlrev_b32_e32 v11, 16, v2
	v_lshlrev_b32_e32 v85, 16, v17
	v_lshlrev_b32_e32 v84, 16, v16
	v_and_b32_e32 v87, 0xffff0000, v17
	v_and_b32_e32 v86, 0xffff0000, v16
	v_lshlrev_b32_e32 v80, 16, v14
	v_and_b32_e32 v81, 0xffff0000, v14
	v_lshlrev_b32_e32 v82, 16, v15
	v_and_b32_e32 v83, 0xffff0000, v15
	v_pk_mul_f32 v[14:15], v[60:61], v[60:61]
	v_pk_fma_f32 v[16:17], v[20:21], v[20:21], v[4:5] op_sel_hi:[1,1,0]
	v_lshlrev_b32_e32 v91, 16, v19
	v_lshlrev_b32_e32 v90, 16, v18
	v_and_b32_e32 v89, 0xffff0000, v19
	v_and_b32_e32 v88, 0xffff0000, v18
	v_pk_fma_f32 v[14:15], v[32:33], v[32:33], v[14:15]
	v_mov_b32_e32 v10, v16
	v_mov_b32_e32 v18, v12
	v_mov_b32_e32 v19, v11
	v_mul_f32_e32 v24, v5, v5
	v_pk_add_f32 v[12:13], v[16:17], v[12:13]
	v_pk_mul_f32 v[16:17], v[10:11], v[18:19]
	v_pk_add_f32 v[14:15], v[14:15], v[14:15] op_sel:[0,1] op_sel_hi:[1,0]
	v_mov_b32_e32 v13, v17
	v_mov_b32_e32 v15, v24
	v_mul_f32_e32 v4, v7, v7
	v_lshlrev_b32_e32 v2, 16, v3
	v_and_b32_e32 v3, 0xffff0000, v3
	v_pk_add_f32 v[12:13], v[12:13], v[14:15]
	v_pk_fma_f32 v[14:15], v[6:7], v[6:7], v[4:5] op_sel_hi:[1,1,0]
	v_mul_f32_e32 v4, v9, v9
	v_mul_f32_e32 v25, v2, v2
	v_mul_f32_e32 v26, v3, v3
	v_pk_fma_f32 v[16:17], v[8:9], v[8:9], v[4:5] op_sel_hi:[1,1,0]
	v_mov_b32_e32 v15, v25
	v_mov_b32_e32 v17, v26
	v_pk_add_f32 v[14:15], v[14:15], v[16:17]
	v_pk_mul_f32 v[16:17], v[86:87], v[86:87]
	v_pk_add_f32 v[12:13], v[12:13], v[14:15]
	v_pk_mul_f32 v[14:15], v[88:89], v[88:89]
	v_pk_add_f32 v[12:13], v[12:13], v[12:13] op_sel:[0,1] op_sel_hi:[1,0]
	v_pk_fma_f32 v[14:15], v[90:91], v[90:91], v[14:15]
	v_mov_b32_e32 v78, v12
	v_pk_add_f32 v[14:15], v[14:15], v[14:15] op_sel:[0,1] op_sel_hi:[1,0]
	v_mov_b32_e32 v19, v79
	v_mov_b32_e32 v18, v14
	v_pk_fma_f32 v[16:17], v[84:85], v[84:85], v[16:17]
	v_pk_add_f32 v[12:13], v[12:13], v[14:15]
	v_pk_mul_f32 v[14:15], v[78:79], v[18:19]
	v_mul_f32_e32 v4, v77, v77
	v_mov_b32_e32 v13, v15
	v_pk_add_f32 v[14:15], v[16:17], v[16:17] op_sel:[0,1] op_sel_hi:[1,0]
	v_mul_f32_e32 v10, v74, v74
	v_mov_b32_e32 v15, v4
	v_mul_f32_e32 v4, v81, v81
	v_pk_add_f32 v[12:13], v[12:13], v[14:15]
	v_pk_fma_f32 v[14:15], v[80:81], v[80:81], v[4:5] op_sel_hi:[1,1,0]
	v_mul_f32_e32 v4, v83, v83
	v_mul_f32_e32 v24, v75, v75
	v_pk_fma_f32 v[16:17], v[82:83], v[82:83], v[4:5] op_sel_hi:[1,1,0]
	v_mov_b32_e32 v15, v10
	v_mov_b32_e32 v17, v24
	v_pk_add_f32 v[14:15], v[14:15], v[16:17]
	v_and_b32_e32 v10, 64, v129
	v_pk_add_f32 v[12:13], v[12:13], v[14:15]
	v_add_u32_e32 v10, 64, v10
	v_add_f32_e32 v4, v12, v13
	v_xor_b32_e32 v12, 1, v129
	v_cmp_lt_i32_e32 vcc, v12, v10
	v_mov_b32_e32 v64, v32
	v_mov_b32_e32 v65, v60
	v_cndmask_b32_e32 v12, v129, v12, vcc
	v_lshlrev_b32_e32 v78, 2, v12
	ds_bpermute_b32 v12, v78, v4
	v_mov_b32_e32 v60, v33
	s_waitcnt lgkmcnt(0)
	v_add_f32_e32 v4, v4, v12
	v_xor_b32_e32 v12, 2, v129
	v_cmp_lt_i32_e32 vcc, v12, v10
	s_nop 1
	v_cndmask_b32_e32 v12, v129, v12, vcc
	v_lshlrev_b32_e32 v138, 2, v12
	ds_bpermute_b32 v12, v138, v4
	s_waitcnt lgkmcnt(0)
	v_add_f32_e32 v4, v4, v12
	v_xor_b32_e32 v12, 4, v129
	v_cmp_lt_i32_e32 vcc, v12, v10
	s_nop 1
	v_cndmask_b32_e32 v12, v129, v12, vcc
	v_lshlrev_b32_e32 v139, 2, v12
	ds_bpermute_b32 v12, v139, v4
	s_waitcnt lgkmcnt(0)
	v_add_f32_e32 v4, v4, v12
	v_xor_b32_e32 v12, 8, v129
	v_cmp_lt_i32_e32 vcc, v12, v10
	s_nop 1
	v_cndmask_b32_e32 v12, v129, v12, vcc
	v_lshlrev_b32_e32 v140, 2, v12
	ds_bpermute_b32 v12, v140, v4
	s_waitcnt lgkmcnt(0)
	v_add_f32_e32 v4, v4, v12
	v_xor_b32_e32 v12, 16, v129
	v_cmp_lt_i32_e32 vcc, v12, v10
	s_nop 1
	v_cndmask_b32_e32 v12, v129, v12, vcc
	v_lshlrev_b32_e32 v141, 2, v12
	ds_bpermute_b32 v12, v141, v4
	s_waitcnt lgkmcnt(0)
	v_add_f32_e32 v4, v4, v12
	v_xor_b32_e32 v12, 32, v129
	v_cmp_lt_i32_e32 vcc, v12, v10
	s_nop 1
	v_cndmask_b32_e32 v10, v129, v12, vcc
	v_lshlrev_b32_e32 v142, 2, v10
	ds_bpermute_b32 v10, v142, v4
	s_waitcnt lgkmcnt(0)
	v_add_f32_e32 v4, v4, v10
	v_fmamk_f32 v4, v4, 0x3a000000, v1
	v_mul_f32_e32 v10, 0x4f800000, v4
	v_cmp_gt_f32_e32 vcc, s28, v4
	s_nop 1
	v_cndmask_b32_e32 v4, v4, v10, vcc
	v_sqrt_f32_e32 v10, v4
	s_nop 0
	v_add_u32_e32 v12, -1, v10
	v_fma_f32 v13, -v12, v10, v4
	v_cmp_ge_f32_e64 s[6:7], 0, v13
	v_add_u32_e32 v13, 1, v10
	s_nop 0
	v_cndmask_b32_e64 v12, v10, v12, s[6:7]
	v_fma_f32 v10, -v13, v10, v4
	v_cmp_lt_f32_e64 s[6:7], 0, v10
	s_nop 1
	v_cndmask_b32_e64 v10, v12, v13, s[6:7]
	v_mul_f32_e32 v12, 0x37800000, v10
	v_cndmask_b32_e32 v10, v10, v12, vcc
	v_cmp_class_f32_e32 vcc, v4, v124
	s_nop 1
	v_cndmask_b32_e32 v4, v10, v4, vcc
	v_div_scale_f32 v10, s[6:7], v4, v4, 1.0
	v_rcp_f32_e32 v12, v10
	s_nop 0
	v_fma_f32 v13, -v10, v12, 1.0
	v_fmac_f32_e32 v12, v13, v12
	v_div_scale_f32 v13, vcc, 1.0, v4, 1.0
	v_mul_f32_e32 v14, v13, v12
	v_fma_f32 v15, -v10, v14, v13
	v_fmac_f32_e32 v14, v15, v12
	v_fma_f32 v10, -v10, v14, v13
	v_div_fmas_f32 v10, v10, v12, v14
	ds_read_b128 v[12:15], v128 offset:8192
	ds_read_b128 v[16:19], v128
	v_div_fixup_f32 v34, v10, v4, 1.0
	v_pk_mul_f32 v[28:29], v[34:35], v[20:21] op_sel_hi:[0,1]
	v_pk_mul_f32 v[30:31], v[34:35], v[22:23] op_sel_hi:[0,1]
	ds_read_b128 v[20:23], v128 offset:9216
	ds_read_b128 v[24:27], v128 offset:1024
	s_waitcnt lgkmcnt(2)
; #define LAS __attribute__((address_space(3)))
; __device__ __forceinline__ unsigned pk2(float lo, float hi) { return f2bf(lo) | (f2bf(hi) << 16); }
; template <bool ROUTER, bool OUT8, bool IN16>
; __device__ __forceinline__ void rms_rows(const Ctx& X, const void* __restrict__ Xin, void* __restrict__ Hv, const LAS float* sh, const LAS float* gs,
;                                          const LAS float* router_w_lds, unsigned* cnt, unsigned* route) {
;     ...
;         for (int j = 0; j < 8; ++j) { const int c = 4 * X.lane + 256 * j;
;             const f32x4 g4 = *(const LAS f32x4*)(gs + c), s4 = *(const LAS f32x4*)(sh + c);
;             const f32x4 h = v[j] * r * g4 + s4;
;             if (OUT8) { const unsigned q_ = pg8::pk4_fp8(h[0] * pg8::A8_SCALE, h[1] * pg8::A8_SCALE, h[2] * pg8::A8_SCALE, h[3] * pg8::A8_SCALE); if (ROUTER) hq[j] = q_; else *(unsigned*)((unsigned char*)Hv + (size_t)t * DM + c) = q_; }
;             else { v2u o; o.x = pk2(h[0], h[1]); o.y = pk2(h[2], h[3]); *(v2u*)((bf16*)Hv + (size_t)t * DM + c) = o; }
;             if (ROUTER) {
; #pragma unroll
;                 for (int e = 0; e < 8; ++e) { const f32x4 w = *(const LAS f32x4*)((const LAS float*)router_w_lds + e * DM + c);
;                     lg[e] += (h[0] * w[0] + h[1] * w[1]) + (h[2] * w[2] + h[3] * w[3]); } }
	v_pk_fma_f32 v[58:59], v[14:15], v[30:31], v[18:19]
	v_pk_fma_f32 v[62:63], v[12:13], v[28:29], v[16:17]
	ds_read_b128 v[12:15], v128 offset:16384
	ds_read_b128 v[16:19], v128 offset:24576
	ds_read_b128 v[28:31], v128 offset:32768
	ds_read_b128 v[66:69], v128 offset:40960
	ds_read_b128 v[70:73], v128 offset:49152
	ds_read_b128 v[102:105], v128 offset:57344
	ds_read_b128 v[106:109], v130 offset:49152
	ds_read_b128 v[110:113], v130 offset:57344
	ds_read_b128 v[92:95], v128 offset:17408
	v_pk_mul_f32 v[64:65], v[34:35], v[64:65] op_sel_hi:[0,1]
	v_pk_mul_f32 v[32:33], v[34:35], v[60:61] op_sel_hi:[0,1]
	s_waitcnt lgkmcnt(9)
	v_pk_fma_f32 v[64:65], v[64:65], v[20:21], v[24:25]
	v_pk_fma_f32 v[60:61], v[32:33], v[22:23], v[26:27]
	s_waitcnt lgkmcnt(8)
	v_mov_b32_e32 v20, v12
	s_waitcnt lgkmcnt(0)
	v_mov_b32_e32 v23, v92
	v_mov_b32_e32 v12, v13
	v_mov_b32_e32 v13, v65
	v_mov_b32_e32 v92, v63
	v_mov_b32_e32 v21, v64
	v_mov_b32_e32 v22, v62
	v_pk_mul_f32 v[12:13], v[12:13], v[92:93]
	v_mov_b32_e32 v24, v63
	v_pk_fma_f32 v[12:13], v[20:21], v[22:23], v[12:13]
	v_mov_b32_e32 v20, v14
	v_mov_b32_e32 v23, v94
	v_mov_b32_e32 v14, v15
	v_mov_b32_e32 v15, v61
	v_mov_b32_e32 v94, v59
	v_mov_b32_e32 v21, v60
	v_mov_b32_e32 v22, v58
	v_pk_mul_f32 v[14:15], v[14:15], v[94:95]
	v_mov_b32_e32 v25, v65
	v_pk_fma_f32 v[14:15], v[20:21], v[22:23], v[14:15]
	v_mov_b32_e32 v22, v62
	v_pk_add_f32 v[20:21], v[12:13], v[14:15]
	ds_read_b128 v[12:15], v128 offset:25600
	v_add_f32_e32 v4, 0, v20
	v_mov_b32_e32 v20, v16
	v_mov_b32_e32 v16, v17
	v_mov_b32_e32 v17, v65
	s_waitcnt lgkmcnt(0)
	v_mov_b32_e32 v23, v12
	v_mov_b32_e32 v12, v63
	v_add_f32_e32 v92, v4, v21
	v_mov_b32_e32 v21, v64
	v_pk_mul_f32 v[12:13], v[16:17], v[12:13]
	v_mov_b32_e32 v16, v18
	v_pk_fma_f32 v[12:13], v[20:21], v[22:23], v[12:13]
	v_mov_b32_e32 v21, v14
	v_mov_b32_e32 v18, v19
	v_mov_b32_e32 v19, v61
	v_mov_b32_e32 v14, v59
	v_mov_b32_e32 v17, v60
	v_mov_b32_e32 v20, v58
	v_pk_mul_f32 v[14:15], v[18:19], v[14:15]
	v_mov_b32_e32 v18, v62
	v_pk_fma_f32 v[14:15], v[16:17], v[20:21], v[14:15]
	v_mov_b32_e32 v20, v29
	v_pk_add_f32 v[16:17], v[12:13], v[14:15]
	ds_read_b128 v[12:15], v128 offset:33792
	v_add_f32_e32 v4, 0, v16
	v_mov_b32_e32 v21, v65
	v_add_f32_e32 v94, v4, v17
	v_mov_b32_e32 v16, v28
	s_waitcnt lgkmcnt(0)
	v_mov_b32_e32 v19, v12
	v_mov_b32_e32 v12, v63
	v_mov_b32_e32 v17, v64
	v_pk_mul_f32 v[12:13], v[20:21], v[12:13]
	v_mov_b32_e32 v20, v31
	v_pk_fma_f32 v[12:13], v[16:17], v[18:19], v[12:13]
	v_mov_b32_e32 v19, v14
	v_mov_b32_e32 v21, v61
	v_mov_b32_e32 v14, v59
	v_mov_b32_e32 v16, v30
	v_mov_b32_e32 v17, v60
	v_mov_b32_e32 v18, v58
	v_pk_mul_f32 v[14:15], v[20:21], v[14:15]
	v_mov_b32_e32 v20, v67
	v_pk_fma_f32 v[14:15], v[16:17], v[18:19], v[14:15]
	v_mov_b32_e32 v21, v65
	v_pk_add_f32 v[16:17], v[12:13], v[14:15]
	ds_read_b128 v[12:15], v128 offset:41984
	v_add_f32_e32 v4, 0, v16
	v_add_f32_e32 v96, v4, v17
	v_mov_b32_e32 v16, v66
	v_mov_b32_e32 v17, v64
	s_waitcnt lgkmcnt(0)
	v_mov_b32_e32 v19, v12
	v_mov_b32_e32 v12, v63
	v_mov_b32_e32 v18, v62
	v_pk_mul_f32 v[12:13], v[20:21], v[12:13]
	v_mov_b32_e32 v20, v69
	v_pk_fma_f32 v[12:13], v[16:17], v[18:19], v[12:13]
	v_mov_b32_e32 v19, v14
	v_mov_b32_e32 v21, v61
	v_mov_b32_e32 v14, v59
	v_mov_b32_e32 v16, v68
	v_mov_b32_e32 v17, v60
	v_mov_b32_e32 v18, v58
	v_pk_mul_f32 v[14:15], v[20:21], v[14:15]
	v_mov_b32_e32 v20, v71
	v_pk_fma_f32 v[14:15], v[16:17], v[18:19], v[14:15]
	v_mov_b32_e32 v21, v65
	v_pk_add_f32 v[16:17], v[12:13], v[14:15]
	ds_read_b128 v[12:15], v128 offset:50176
	v_add_f32_e32 v4, 0, v16
	v_add_f32_e32 v98, v4, v17
	v_mov_b32_e32 v16, v70
	v_mov_b32_e32 v17, v64
	s_waitcnt lgkmcnt(0)
	v_mov_b32_e32 v19, v12
	v_mov_b32_e32 v12, v63
	v_mov_b32_e32 v18, v62
	v_pk_mul_f32 v[12:13], v[20:21], v[12:13]
	v_mov_b32_e32 v20, v73
	v_pk_fma_f32 v[12:13], v[16:17], v[18:19], v[12:13]
	v_mov_b32_e32 v19, v14
	v_mov_b32_e32 v21, v61
	v_mov_b32_e32 v14, v59
	v_mov_b32_e32 v16, v72
	v_mov_b32_e32 v17, v60
	v_mov_b32_e32 v18, v58
	v_pk_mul_f32 v[14:15], v[20:21], v[14:15]
	v_mov_b32_e32 v20, v103
	v_pk_fma_f32 v[14:15], v[16:17], v[18:19], v[14:15]
	v_mov_b32_e32 v21, v65
	v_pk_add_f32 v[16:17], v[12:13], v[14:15]
	ds_read_b128 v[12:15], v128 offset:58368
	v_add_f32_e32 v4, 0, v16
	v_add_f32_e32 v100, v4, v17
	v_mov_b32_e32 v16, v102
	v_mov_b32_e32 v17, v64
	s_waitcnt lgkmcnt(0)
	v_mov_b32_e32 v19, v12
	v_mov_b32_e32 v12, v63
	v_mov_b32_e32 v18, v62
	v_pk_mul_f32 v[12:13], v[20:21], v[12:13]
	v_mov_b32_e32 v20, v105
	v_pk_fma_f32 v[12:13], v[16:17], v[18:19], v[12:13]
	v_mov_b32_e32 v19, v14
	v_mov_b32_e32 v21, v61
	v_mov_b32_e32 v14, v59
	v_mov_b32_e32 v16, v104
	v_mov_b32_e32 v17, v60
	v_mov_b32_e32 v18, v58
	v_pk_mul_f32 v[14:15], v[20:21], v[14:15]
	v_mov_b32_e32 v20, v62
	v_pk_fma_f32 v[14:15], v[16:17], v[18:19], v[14:15]
	ds_read_b128 v[16:19], v131 offset:57344
	v_pk_add_f32 v[12:13], v[12:13], v[14:15]
	v_mov_b32_e32 v21, v64
	v_add_f32_e32 v4, 0, v12
	v_add_f32_e32 v102, v4, v13
	ds_read_b128 v[12:15], v131 offset:49152
	v_mov_b32_e32 v22, v106
	v_mov_b32_e32 v28, v59
	v_mov_b32_e32 v29, v61
	v_mov_b32_e32 v26, v108
	s_waitcnt lgkmcnt(0)
; #define LAS __attribute__((address_space(3)))
; __device__ __forceinline__ unsigned pk2(float lo, float hi) { return f2bf(lo) | (f2bf(hi) << 16); }
; template <bool ROUTER, bool OUT8, bool IN16>
; __device__ __forceinline__ void rms_rows(const Ctx& X, const void* __restrict__ Xin, void* __restrict__ Hv, const LAS float* sh, const LAS float* gs,
;                                          const LAS float* router_w_lds, unsigned* cnt, unsigned* route) {
;     ...
;         for (int j = 0; j < 8; ++j) { const int c = 4 * X.lane + 256 * j;
;             const f32x4 g4 = *(const LAS f32x4*)(gs + c), s4 = *(const LAS f32x4*)(sh + c);
;             const f32x4 h = v[j] * r * g4 + s4;
;             if (OUT8) { const unsigned q_ = pg8::pk4_fp8(h[0] * pg8::A8_SCALE, h[1] * pg8::A8_SCALE, h[2] * pg8::A8_SCALE, h[3] * pg8::A8_SCALE); if (ROUTER) hq[j] = q_; else *(unsigned*)((unsigned char*)Hv + (size_t)t * DM + c) = q_; }
;             else { v2u o; o.x = pk2(h[0], h[1]); o.y = pk2(h[2], h[3]); *(v2u*)((bf16*)Hv + (size_t)t * DM + c) = o; }
;             if (ROUTER) {
; #pragma unroll
;                 for (int e = 0; e < 8; ++e) { const f32x4 w = *(const LAS f32x4*)((const LAS float*)router_w_lds + e * DM + c);
;                     lg[e] += (h[0] * w[0] + h[1] * w[1]) + (h[2] * w[2] + h[3] * w[3]); } }
	v_mov_b32_e32 v23, v12
	v_mov_b32_e32 v12, v107
	v_pk_mul_f32 v[12:13], v[24:25], v[12:13]
	v_mov_b32_e32 v27, v14
	v_mov_b32_e32 v14, v109
	v_pk_fma_f32 v[12:13], v[20:21], v[22:23], v[12:13]
	v_mov_b32_e32 v22, v58
	v_mov_b32_e32 v23, v60
	v_pk_mul_f32 v[14:15], v[28:29], v[14:15]
	v_pk_mul_f32 v[2:3], v[34:35], v[2:3] op_sel_hi:[0,1]
	v_pk_fma_f32 v[14:15], v[22:23], v[26:27], v[14:15]
	s_nop 0
	v_pk_add_f32 v[12:13], v[12:13], v[14:15]
	s_nop 0
	v_add_f32_e32 v4, 0, v12
	v_add_f32_e32 v104, v4, v13
	v_mov_b32_e32 v13, v16
	v_mov_b32_e32 v16, v111
	v_mov_b32_e32 v12, v110
	v_pk_mul_f32 v[14:15], v[24:25], v[16:17]
	s_nop 0
	v_pk_fma_f32 v[12:13], v[20:21], v[12:13], v[14:15]
	v_mov_b32_e32 v15, v18
	v_mov_b32_e32 v18, v113
	v_mov_b32_e32 v14, v112
	v_pk_mul_f32 v[16:17], v[28:29], v[18:19]
	v_pk_mul_f32 v[20:21], v[34:35], v[6:7] op_sel_hi:[0,1]
	v_pk_fma_f32 v[14:15], v[22:23], v[14:15], v[16:17]
	v_pk_mul_f32 v[22:23], v[34:35], v[8:9] op_sel_hi:[0,1]
	v_pk_add_f32 v[12:13], v[12:13], v[14:15]
	s_nop 0
	v_add_f32_e32 v4, 0, v12
	v_add_f32_e32 v106, v4, v13
	ds_read_b128 v[12:15], v128 offset:10240
	ds_read_b128 v[16:19], v128 offset:2048
	ds_read_b128 v[6:9], v128 offset:18432
	ds_read_b128 v[144:147], v128 offset:11264
	ds_read_b128 v[148:151], v128 offset:3072
	ds_read_b128 v[30:33], v128 offset:19456
	ds_read_b128 v[70:73], v128 offset:59392
	ds_read_b128 v[26:29], v128 offset:27648
	s_waitcnt lgkmcnt(6)
	v_pk_fma_f32 v[66:67], v[22:23], v[14:15], v[18:19]
	v_pk_fma_f32 v[68:69], v[20:21], v[12:13], v[16:17]
	s_waitcnt lgkmcnt(5)
	v_pk_mul_f32 v[12:13], v[66:67], v[8:9]
	v_pk_mul_f32 v[14:15], v[68:69], v[6:7]
	ds_read_b128 v[6:9], v128 offset:26624
	v_pk_mov_b32 v[16:17], v[14:15], v[12:13] op_sel:[1,0]
	v_mov_b32_e32 v15, v13
	v_pk_add_f32 v[122:123], v[16:17], v[14:15]
	ds_read_b128 v[22:25], v128 offset:35840
	s_waitcnt lgkmcnt(1)
	v_pk_mul_f32 v[12:13], v[66:67], v[8:9]
	v_pk_mul_f32 v[14:15], v[68:69], v[6:7]
	ds_read_b128 v[6:9], v128 offset:34816
	v_pk_mov_b32 v[16:17], v[14:15], v[12:13] op_sel:[1,0]
	v_mov_b32_e32 v15, v13
	v_pk_add_f32 v[120:121], v[16:17], v[14:15]
	ds_read_b128 v[18:21], v128 offset:44032
	s_waitcnt lgkmcnt(1)
	v_pk_mul_f32 v[12:13], v[66:67], v[8:9]
	v_pk_mul_f32 v[14:15], v[68:69], v[6:7]
	ds_read_b128 v[6:9], v128 offset:43008
	v_pk_mov_b32 v[16:17], v[14:15], v[12:13] op_sel:[1,0]
	v_mov_b32_e32 v15, v13
	v_pk_add_f32 v[118:119], v[16:17], v[14:15]
	ds_read_b128 v[152:155], v132 offset:57344
	s_waitcnt lgkmcnt(1)
	v_pk_mul_f32 v[12:13], v[66:67], v[8:9]
	v_pk_mul_f32 v[14:15], v[68:69], v[6:7]
	ds_read_b128 v[6:9], v128 offset:51200
	v_pk_mov_b32 v[16:17], v[14:15], v[12:13] op_sel:[1,0]
	v_mov_b32_e32 v15, v13
	v_pk_add_f32 v[116:117], v[16:17], v[14:15]
	ds_read_b128 v[14:17], v128 offset:52224
	s_waitcnt lgkmcnt(1)
	v_pk_mul_f32 v[8:9], v[66:67], v[8:9]
	v_pk_mul_f32 v[6:7], v[68:69], v[6:7]
	v_mov_b32_e32 v4, v11
	v_pk_mov_b32 v[12:13], v[6:7], v[8:9] op_sel:[1,0]
	v_mov_b32_e32 v7, v9
	v_pk_add_f32 v[114:115], v[12:13], v[6:7]
	ds_read_b128 v[6:9], v128 offset:60416
	v_pk_mul_f32 v[12:13], v[66:67], v[72:73]
	v_pk_mul_f32 v[108:109], v[68:69], v[70:71]
	ds_read_b128 v[70:73], v132 offset:49152
	v_pk_mov_b32 v[110:111], v[108:109], v[12:13] op_sel:[1,0]
	v_mov_b32_e32 v109, v13
	v_pk_add_f32 v[112:113], v[110:111], v[108:109]
	v_pk_mul_f32 v[4:5], v[34:35], v[4:5] op_sel_hi:[0,1]
	s_waitcnt lgkmcnt(0)
	v_pk_mul_f32 v[12:13], v[66:67], v[72:73]
	v_pk_mul_f32 v[70:71], v[68:69], v[70:71]
	v_pk_add_f32 v[122:123], v[122:123], v[122:123] op_sel:[0,1] op_sel_hi:[1,0]
	v_pk_mov_b32 v[72:73], v[70:71], v[12:13] op_sel:[1,0]
	v_mov_b32_e32 v71, v13
	v_pk_add_f32 v[110:111], v[72:73], v[70:71]
	v_pk_mul_f32 v[12:13], v[66:67], v[154:155]
	v_pk_mul_f32 v[70:71], v[68:69], v[152:153]
	v_mov_b32_e32 v152, v90
	v_pk_mov_b32 v[72:73], v[70:71], v[12:13] op_sel:[1,0]
	v_mov_b32_e32 v71, v13
	v_pk_add_f32 v[108:109], v[72:73], v[70:71]
	v_pk_fma_f32 v[70:71], v[2:3], v[146:147], v[150:151]
	v_pk_fma_f32 v[72:73], v[4:5], v[144:145], v[148:149]
	ds_read_b128 v[10:13], v133 offset:49152
	ds_read_b128 v[2:5], v133 offset:57344
	ds_read_b128 v[144:147], v128 offset:12288
	ds_read_b128 v[148:151], v128 offset:4096
	v_mov_b32_e32 v153, v88
	v_pk_mul_f32 v[164:165], v[34:35], v[152:153] op_sel_hi:[0,1]
	ds_read_b128 v[152:155], v128 offset:20480
	ds_read_b128 v[156:159], v128 offset:13312
	ds_read_b128 v[160:163], v128 offset:5120
	v_mov_b32_e32 v88, v91
	s_waitcnt lgkmcnt(3)
	v_pk_fma_f32 v[90:91], v[164:165], v[144:145], v[148:149]
	v_pk_mul_f32 v[88:89], v[34:35], v[88:89] op_sel_hi:[0,1]
	s_waitcnt lgkmcnt(2)
	v_mul_f32_e32 v76, v91, v153
	v_mul_f32_e32 v93, v90, v152
	v_mov_b32_e32 v123, v76
	v_mul_f32_e32 v76, v73, v31
	v_pk_add_f32 v[92:93], v[92:93], v[122:123]
	v_pk_fma_f32 v[122:123], v[72:73], v[30:31], v[76:77] op_sel_hi:[1,1,0]
	v_mul_f32_e32 v30, v71, v33
	v_pk_fma_f32 v[88:89], v[88:89], v[146:147], v[150:151]
	ds_read_b128 v[144:147], v128 offset:21504
	v_pk_fma_f32 v[148:149], v[70:71], v[32:33], v[30:31] op_sel_hi:[1,1,0]
	ds_read_b128 v[30:33], v128 offset:28672
	v_mul_f32_e32 v95, v88, v154
	v_mul_f32_e32 v97, v89, v155
	v_mov_b32_e32 v123, v95
	v_mov_b32_e32 v149, v97
	s_waitcnt lgkmcnt(0)
	v_mul_f32_e32 v95, v90, v30
	v_mul_f32_e32 v76, v91, v31
	v_mul_f32_e32 v97, v88, v32
	v_pk_add_f32 v[30:31], v[120:121], v[120:121] op_sel:[0,1] op_sel_hi:[1,0]
	v_mul_f32_e32 v32, v73, v27
	v_mul_f32_e32 v99, v89, v33
	v_mov_b32_e32 v31, v76
	v_pk_fma_f32 v[32:33], v[72:73], v[26:27], v[32:33] op_sel_hi:[1,1,0]
	v_mul_f32_e32 v26, v71, v29
	v_pk_add_f32 v[30:31], v[94:95], v[30:31]
	v_pk_fma_f32 v[94:95], v[70:71], v[28:29], v[26:27] op_sel_hi:[1,1,0]
	ds_read_b128 v[26:29], v128 offset:36864
	v_mov_b32_e32 v33, v97
	v_mov_b32_e32 v95, v99
	v_pk_add_f32 v[122:123], v[122:123], v[148:149]
	v_pk_add_f32 v[32:33], v[32:33], v[94:95]
	v_pk_add_f32 v[92:93], v[92:93], v[122:123]
	v_pk_add_f32 v[32:33], v[30:31], v[32:33]
	ds_read_b128 v[120:123], v128 offset:37888
	s_waitcnt lgkmcnt(1)
; #define LAS __attribute__((address_space(3)))
; __device__ __forceinline__ unsigned pk2(float lo, float hi) { return f2bf(lo) | (f2bf(hi) << 16); }
; template <bool ROUTER, bool OUT8, bool IN16>
; __device__ __forceinline__ void rms_rows(const Ctx& X, const void* __restrict__ Xin, void* __restrict__ Hv, const LAS float* sh, const LAS float* gs,
;                                          const LAS float* router_w_lds, unsigned* cnt, unsigned* route) {
;     ...
;         for (int j = 0; j < 8; ++j) { const int c = 4 * X.lane + 256 * j;
;             const f32x4 g4 = *(const LAS f32x4*)(gs + c), s4 = *(const LAS f32x4*)(sh + c);
;             const f32x4 h = v[j] * r * g4 + s4;
;             if (OUT8) { const unsigned q_ = pg8::pk4_fp8(h[0] * pg8::A8_SCALE, h[1] * pg8::A8_SCALE, h[2] * pg8::A8_SCALE, h[3] * pg8::A8_SCALE); if (ROUTER) hq[j] = q_; else *(unsigned*)((unsigned char*)Hv + (size_t)t * DM + c) = q_; }
;             else { v2u o; o.x = pk2(h[0], h[1]); o.y = pk2(h[2], h[3]); *(v2u*)((bf16*)Hv + (size_t)t * DM + c) = o; }
;             if (ROUTER) {
; #pragma unroll
;                 for (int e = 0; e < 8; ++e) { const f32x4 w = *(const LAS f32x4*)((const LAS float*)router_w_lds + e * DM + c);
;                     lg[e] += (h[0] * w[0] + h[1] * w[1]) + (h[2] * w[2] + h[3] * w[3]); } }
	v_mul_f32_e32 v31, v88, v28
	v_mul_f32_e32 v28, v73, v23
	v_mul_f32_e32 v97, v90, v26
	v_mul_f32_e32 v30, v91, v27
	v_mul_f32_e32 v76, v89, v29
	v_pk_add_f32 v[26:27], v[118:119], v[118:119] op_sel:[0,1] op_sel_hi:[1,0]
	v_pk_fma_f32 v[28:29], v[72:73], v[22:23], v[28:29] op_sel_hi:[1,1,0]
	v_mul_f32_e32 v22, v71, v25
	v_mov_b32_e32 v27, v30
	v_mov_b32_e32 v29, v31
	v_pk_fma_f32 v[30:31], v[70:71], v[24:25], v[22:23] op_sel_hi:[1,1,0]
	ds_read_b128 v[22:25], v128 offset:45056
	v_mov_b32_e32 v31, v76
	v_pk_add_f32 v[26:27], v[96:97], v[26:27]
	v_pk_add_f32 v[28:29], v[28:29], v[30:31]
	ds_read_b128 v[94:97], v128 offset:46080
	v_pk_add_f32 v[30:31], v[26:27], v[28:29]
	s_waitcnt lgkmcnt(1)
	v_mul_f32_e32 v27, v88, v24
	v_mul_f32_e32 v24, v73, v19
	v_mul_f32_e32 v99, v90, v22
	v_mul_f32_e32 v26, v91, v23
	v_mul_f32_e32 v28, v89, v25
	v_pk_add_f32 v[22:23], v[116:117], v[116:117] op_sel:[0,1] op_sel_hi:[1,0]
	v_pk_fma_f32 v[24:25], v[72:73], v[18:19], v[24:25] op_sel_hi:[1,1,0]
	v_mul_f32_e32 v18, v71, v21
	v_mov_b32_e32 v23, v26
	v_mov_b32_e32 v25, v27
	v_pk_fma_f32 v[26:27], v[70:71], v[20:21], v[18:19] op_sel_hi:[1,1,0]
	ds_read_b128 v[18:21], v128 offset:53248
	ds_read_b128 v[116:119], v128 offset:54272
	v_mov_b32_e32 v27, v28
	v_pk_add_f32 v[22:23], v[98:99], v[22:23]
	v_pk_add_f32 v[24:25], v[24:25], v[26:27]
	s_waitcnt lgkmcnt(1)
	v_mul_f32_e32 v101, v90, v18
	v_pk_add_f32 v[28:29], v[22:23], v[24:25]
	v_mul_f32_e32 v23, v88, v20
	v_mul_f32_e32 v20, v73, v15
	v_mul_f32_e32 v22, v91, v19
	v_mul_f32_e32 v24, v89, v21
	v_pk_add_f32 v[18:19], v[114:115], v[114:115] op_sel:[0,1] op_sel_hi:[1,0]
	v_pk_fma_f32 v[20:21], v[72:73], v[14:15], v[20:21] op_sel_hi:[1,1,0]
	v_mul_f32_e32 v14, v71, v17
	v_mov_b32_e32 v19, v22
	v_mov_b32_e32 v21, v23
	v_pk_fma_f32 v[22:23], v[70:71], v[16:17], v[14:15] op_sel_hi:[1,1,0]
	ds_read_b128 v[14:17], v128 offset:61440
	v_mov_b32_e32 v23, v24
	v_pk_add_f32 v[18:19], v[100:101], v[18:19]
	v_pk_add_f32 v[20:21], v[20:21], v[22:23]
	ds_read_b128 v[98:101], v128 offset:62464
	v_pk_add_f32 v[26:27], v[18:19], v[20:21]
	s_waitcnt lgkmcnt(1)
	v_mul_f32_e32 v19, v88, v16
	v_mul_f32_e32 v16, v73, v7
	v_mul_f32_e32 v103, v90, v14
	v_mul_f32_e32 v18, v91, v15
	v_mul_f32_e32 v20, v89, v17
	v_pk_add_f32 v[14:15], v[112:113], v[112:113] op_sel:[0,1] op_sel_hi:[1,0]
	v_pk_fma_f32 v[16:17], v[72:73], v[6:7], v[16:17] op_sel_hi:[1,1,0]
	v_mul_f32_e32 v6, v71, v9
	ds_read_b128 v[148:151], v128 offset:29696
	v_mov_b32_e32 v15, v18
	v_mov_b32_e32 v17, v19
	v_pk_fma_f32 v[18:19], v[70:71], v[8:9], v[6:7] op_sel_hi:[1,1,0]
	ds_read_b128 v[6:9], v134 offset:49152
	v_mov_b32_e32 v19, v20
	v_pk_add_f32 v[14:15], v[102:103], v[14:15]
	v_pk_add_f32 v[16:17], v[16:17], v[18:19]
	v_mov_b32_e32 v76, v79
	v_pk_add_f32 v[24:25], v[14:15], v[16:17]
	ds_read_b128 v[14:17], v134 offset:57344
	s_waitcnt lgkmcnt(1)
	v_mul_f32_e32 v19, v88, v8
	v_mul_f32_e32 v8, v73, v11
	v_mul_f32_e32 v20, v89, v9
	v_pk_fma_f32 v[8:9], v[72:73], v[10:11], v[8:9] op_sel_hi:[1,1,0]
	v_mul_f32_e32 v10, v71, v13
	v_mul_f32_e32 v105, v90, v6
	v_mul_f32_e32 v18, v91, v7
	v_pk_add_f32 v[6:7], v[110:111], v[110:111] op_sel:[0,1] op_sel_hi:[1,0]
	v_pk_fma_f32 v[10:11], v[70:71], v[12:13], v[10:11] op_sel_hi:[1,1,0]
	v_mov_b32_e32 v7, v18
	v_mov_b32_e32 v9, v19
	v_mov_b32_e32 v11, v20
	v_pk_add_f32 v[6:7], v[104:105], v[6:7]
	v_pk_add_f32 v[8:9], v[8:9], v[10:11]
	s_waitcnt lgkmcnt(0)
	v_mul_f32_e32 v10, v89, v17
	v_pk_add_f32 v[20:21], v[6:7], v[8:9]
	v_mul_f32_e32 v8, v91, v15
	v_pk_add_f32 v[6:7], v[108:109], v[108:109] op_sel:[0,1] op_sel_hi:[1,0]
	v_mul_f32_e32 v9, v88, v16
	v_mov_b32_e32 v7, v8
	v_mul_f32_e32 v8, v73, v3
	v_pk_fma_f32 v[2:3], v[72:73], v[2:3], v[8:9] op_sel_hi:[1,1,0]
	v_mul_f32_e32 v8, v71, v5
	v_pk_fma_f32 v[4:5], v[70:71], v[4:5], v[8:9] op_sel_hi:[1,1,0]
	v_mul_f32_e32 v107, v90, v14
	v_mov_b32_e32 v3, v9
	v_mov_b32_e32 v5, v10
	v_pk_add_f32 v[6:7], v[106:107], v[6:7]
	v_pk_add_f32 v[2:3], v[2:3], v[4:5]
	v_pk_mul_f32 v[16:17], v[34:35], v[80:81] op_sel_hi:[0,1]
	v_pk_add_f32 v[18:19], v[6:7], v[2:3]
	v_mov_b32_e32 v2, v84
	v_mov_b32_e32 v3, v86
	v_mov_b32_e32 v86, v85
	v_pk_mul_f32 v[2:3], v[34:35], v[2:3] op_sel_hi:[0,1]
	v_pk_mul_f32 v[4:5], v[34:35], v[86:87] op_sel_hi:[0,1]
	v_pk_fma_f32 v[6:7], v[4:5], v[158:159], v[162:163]
	v_pk_fma_f32 v[8:9], v[2:3], v[156:157], v[160:161]
	v_pk_mul_f32 v[2:3], v[6:7], v[146:147]
	v_pk_mul_f32 v[4:5], v[8:9], v[144:145]
	v_pk_mul_f32 v[12:13], v[8:9], v[98:99]
	v_pk_mov_b32 v[10:11], v[4:5], v[2:3] op_sel:[1,0]
	v_mov_b32_e32 v5, v3
	v_pk_add_f32 v[86:87], v[10:11], v[4:5]
	v_pk_mul_f32 v[2:3], v[6:7], v[150:151]
	v_pk_mul_f32 v[4:5], v[8:9], v[148:149]
	v_pk_add_f32 v[32:33], v[32:33], v[32:33] op_sel:[0,1] op_sel_hi:[1,0]
	v_pk_mov_b32 v[10:11], v[4:5], v[2:3] op_sel:[1,0]
	v_mov_b32_e32 v5, v3
	v_pk_add_f32 v[110:111], v[10:11], v[4:5]
	v_pk_mul_f32 v[2:3], v[6:7], v[122:123]
	v_pk_mul_f32 v[4:5], v[8:9], v[120:121]
	v_pk_add_f32 v[30:31], v[30:31], v[30:31] op_sel:[0,1] op_sel_hi:[1,0]
	v_pk_mov_b32 v[10:11], v[4:5], v[2:3] op_sel:[1,0]
	v_mov_b32_e32 v5, v3
	v_pk_add_f32 v[112:113], v[10:11], v[4:5]
	v_pk_mul_f32 v[2:3], v[6:7], v[96:97]
	v_pk_mul_f32 v[4:5], v[8:9], v[94:95]
	v_pk_add_f32 v[28:29], v[28:29], v[28:29] op_sel:[0,1] op_sel_hi:[1,0]
	v_pk_mov_b32 v[10:11], v[4:5], v[2:3] op_sel:[1,0]
	v_mov_b32_e32 v5, v3
	v_pk_add_f32 v[114:115], v[10:11], v[4:5]
	v_pk_mul_f32 v[2:3], v[6:7], v[118:119]
	v_pk_mul_f32 v[4:5], v[8:9], v[116:117]
	v_pk_add_f32 v[26:27], v[26:27], v[26:27] op_sel:[0,1] op_sel_hi:[1,0]
	v_pk_mov_b32 v[10:11], v[4:5], v[2:3] op_sel:[1,0]
	v_mov_b32_e32 v5, v3
	v_pk_add_f32 v[116:117], v[10:11], v[4:5]
	v_pk_mul_f32 v[10:11], v[6:7], v[100:101]
	ds_read_b128 v[2:5], v135 offset:49152
	v_pk_mov_b32 v[14:15], v[12:13], v[10:11] op_sel:[1,0]
	v_mov_b32_e32 v13, v11
	v_pk_add_f32 v[118:119], v[14:15], v[12:13]
	ds_read_b128 v[10:13], v135 offset:57344
	s_waitcnt lgkmcnt(1)
; #define LAS __attribute__((address_space(3)))
; __device__ __forceinline__ unsigned pk2(float lo, float hi) { return f2bf(lo) | (f2bf(hi) << 16); }
; template <bool ROUTER, bool OUT8, bool IN16>
; __device__ __forceinline__ void rms_rows(const Ctx& X, const void* __restrict__ Xin, void* __restrict__ Hv, const LAS float* sh, const LAS float* gs,
;                                          const LAS float* router_w_lds, unsigned* cnt, unsigned* route) {
;     ...
;         for (int j = 0; j < 8; ++j) { const int c = 4 * X.lane + 256 * j;
;             const f32x4 g4 = *(const LAS f32x4*)(gs + c), s4 = *(const LAS f32x4*)(sh + c);
;             const f32x4 h = v[j] * r * g4 + s4;
;             if (OUT8) { const unsigned q_ = pg8::pk4_fp8(h[0] * pg8::A8_SCALE, h[1] * pg8::A8_SCALE, h[2] * pg8::A8_SCALE, h[3] * pg8::A8_SCALE); if (ROUTER) hq[j] = q_; else *(unsigned*)((unsigned char*)Hv + (size_t)t * DM + c) = q_; }
;             else { v2u o; o.x = pk2(h[0], h[1]); o.y = pk2(h[2], h[3]); *(v2u*)((bf16*)Hv + (size_t)t * DM + c) = o; }
;             if (ROUTER) {
; #pragma unroll
;                 for (int e = 0; e < 8; ++e) { const f32x4 w = *(const LAS f32x4*)((const LAS float*)router_w_lds + e * DM + c);
;                     lg[e] += (h[0] * w[0] + h[1] * w[1]) + (h[2] * w[2] + h[3] * w[3]); } }
;         }
;         if (ROUTER) {
; #pragma unroll
;             for (int e = 0; e < 8; ++e) lg[e] = wave_sum(lg[e]);
	v_pk_mul_f32 v[4:5], v[6:7], v[4:5]
	v_pk_mul_f32 v[2:3], v[8:9], v[2:3]
	v_pk_add_f32 v[24:25], v[24:25], v[24:25] op_sel:[0,1] op_sel_hi:[1,0]
	v_pk_mov_b32 v[14:15], v[2:3], v[4:5] op_sel:[1,0]
	v_mov_b32_e32 v3, v5
	v_pk_add_f32 v[84:85], v[14:15], v[2:3]
	s_waitcnt lgkmcnt(0)
	v_pk_mul_f32 v[2:3], v[6:7], v[12:13]
	v_pk_mul_f32 v[4:5], v[8:9], v[10:11]
	v_pk_add_f32 v[20:21], v[20:21], v[20:21] op_sel:[0,1] op_sel_hi:[1,0]
	v_pk_mov_b32 v[10:11], v[4:5], v[2:3] op_sel:[1,0]
	v_mov_b32_e32 v5, v3
	v_pk_add_f32 v[22:23], v[10:11], v[4:5]
	ds_read_b128 v[2:5], v128 offset:14336
	ds_read_b128 v[12:15], v128 offset:6144
	v_pk_mul_f32 v[10:11], v[34:35], v[82:83] op_sel_hi:[0,1]
	ds_read_b128 v[80:83], v128 offset:15360
	ds_read_b128 v[94:97], v128 offset:7168
	v_pk_add_f32 v[18:19], v[18:19], v[18:19] op_sel:[0,1] op_sel_hi:[1,0]
	v_pk_add_f32 v[22:23], v[22:23], v[22:23] op_sel:[0,1] op_sel_hi:[1,0]
	s_waitcnt lgkmcnt(2)
	v_pk_fma_f32 v[10:11], v[10:11], v[4:5], v[14:15]
	v_pk_fma_f32 v[14:15], v[16:17], v[2:3], v[12:13]
	ds_read_b128 v[98:101], v136 offset:49152
	ds_read_b128 v[2:5], v136 offset:57344
	ds_read_b128 v[102:105], v128 offset:22528
	ds_read_b128 v[106:109], v128 offset:23552
	v_pk_mul_f32 v[16:17], v[34:35], v[76:77] op_sel_hi:[0,1]
	s_waitcnt lgkmcnt(4)
	v_pk_fma_f32 v[16:17], v[16:17], v[80:81], v[94:95]
	v_pk_mul_f32 v[12:13], v[34:35], v[74:75] op_sel_hi:[0,1]
	v_pk_add_f32 v[74:75], v[92:93], v[92:93] op_sel:[0,1] op_sel_hi:[1,0]
	s_waitcnt lgkmcnt(0)
	v_mul_f32_e32 v34, v16, v106
	v_pk_fma_f32 v[12:13], v[12:13], v[82:83], v[96:97]
	v_mul_f32_e32 v79, v17, v107
	v_mov_b32_e32 v75, v34
	v_pk_add_f32 v[76:77], v[86:87], v[86:87] op_sel:[0,1] op_sel_hi:[1,0]
	v_mul_f32_e32 v34, v15, v103
	v_mul_f32_e32 v80, v12, v108
	v_mov_b32_e32 v77, v79
	v_pk_fma_f32 v[92:93], v[14:15], v[102:103], v[34:35] op_sel_hi:[1,1,0]
	v_pk_add_f32 v[86:87], v[74:75], v[76:77]
	v_mov_b32_e32 v93, v80
	ds_read_b128 v[74:77], v128 offset:30720
	ds_read_b128 v[80:83], v128 offset:31744
	v_mul_f32_e32 v34, v11, v105
	v_mul_f32_e32 v96, v13, v109
	v_pk_fma_f32 v[94:95], v[10:11], v[104:105], v[34:35] op_sel_hi:[1,1,0]
	s_waitcnt lgkmcnt(0)
	v_mul_f32_e32 v34, v16, v80
	v_mov_b32_e32 v95, v96
	v_mul_f32_e32 v79, v17, v81
	v_mov_b32_e32 v33, v34
	v_pk_add_f32 v[80:81], v[110:111], v[110:111] op_sel:[0,1] op_sel_hi:[1,0]
	v_mul_f32_e32 v34, v15, v75
	v_pk_add_f32 v[92:93], v[92:93], v[94:95]
	v_mul_f32_e32 v82, v12, v82
	v_mov_b32_e32 v81, v79
	v_pk_fma_f32 v[74:75], v[14:15], v[74:75], v[34:35] op_sel_hi:[1,1,0]
	v_pk_add_f32 v[86:87], v[86:87], v[92:93]
	v_mul_f32_e32 v96, v13, v83
	v_pk_add_f32 v[32:33], v[32:33], v[80:81]
	v_mov_b32_e32 v75, v82
	ds_read_b128 v[80:83], v128 offset:38912
	ds_read_b128 v[92:95], v128 offset:39936
	v_mul_f32_e32 v34, v11, v77
	v_pk_fma_f32 v[76:77], v[10:11], v[76:77], v[34:35] op_sel_hi:[1,1,0]
	s_waitcnt lgkmcnt(0)
	v_mul_f32_e32 v34, v17, v93
	v_mov_b32_e32 v77, v96
	v_pk_add_f32 v[74:75], v[74:75], v[76:77]
	v_mul_f32_e32 v79, v13, v95
	v_pk_add_f32 v[96:97], v[32:33], v[74:75]
	v_mul_f32_e32 v32, v16, v92
	v_mov_b32_e32 v31, v32
	v_pk_add_f32 v[32:33], v[112:113], v[112:113] op_sel:[0,1] op_sel_hi:[1,0]
	v_mul_f32_e32 v74, v12, v94
	v_mov_b32_e32 v33, v34
	v_pk_add_f32 v[92:93], v[30:31], v[32:33]
	v_mul_f32_e32 v30, v15, v81
	v_pk_fma_f32 v[80:81], v[14:15], v[80:81], v[30:31] op_sel_hi:[1,1,0]
	v_mul_f32_e32 v30, v11, v83
	v_mov_b32_e32 v81, v74
	v_pk_fma_f32 v[82:83], v[10:11], v[82:83], v[30:31] op_sel_hi:[1,1,0]
	ds_read_b128 v[30:33], v128 offset:47104
	ds_read_b128 v[74:77], v128 offset:48128
	v_mov_b32_e32 v83, v79
	v_pk_add_f32 v[80:81], v[80:81], v[82:83]
	s_waitcnt lgkmcnt(0)
	v_mul_f32_e32 v74, v16, v74
	v_mul_f32_e32 v79, v17, v75
	v_mov_b32_e32 v29, v74
	v_pk_add_f32 v[74:75], v[114:115], v[114:115] op_sel:[0,1] op_sel_hi:[1,0]
	v_pk_add_f32 v[80:81], v[92:93], v[80:81]
	v_mov_b32_e32 v75, v79
	v_add_f32_e32 v34, v80, v81
	v_pk_add_f32 v[80:81], v[28:29], v[74:75]
	v_mul_f32_e32 v28, v15, v31
	v_mul_f32_e32 v76, v12, v76
	v_pk_fma_f32 v[82:83], v[14:15], v[30:31], v[28:29] op_sel_hi:[1,1,0]
	v_mul_f32_e32 v28, v11, v33
	v_mul_f32_e32 v92, v13, v77
	v_mov_b32_e32 v83, v76
	v_pk_fma_f32 v[32:33], v[10:11], v[32:33], v[28:29] op_sel_hi:[1,1,0]
	ds_read_b128 v[28:31], v128 offset:55296
	ds_read_b128 v[74:77], v128 offset:56320
	v_mov_b32_e32 v33, v92
	v_pk_add_f32 v[32:33], v[82:83], v[32:33]
	s_waitcnt lgkmcnt(0)
	v_mul_f32_e32 v82, v13, v77
	v_pk_add_f32 v[32:33], v[80:81], v[32:33]
	v_mul_f32_e32 v80, v12, v76
	v_add_f32_e32 v79, v32, v33
	v_mul_f32_e32 v32, v16, v74
	v_mul_f32_e32 v74, v17, v75
	v_mov_b32_e32 v27, v32
	v_pk_add_f32 v[32:33], v[116:117], v[116:117] op_sel:[0,1] op_sel_hi:[1,0]
	s_nop 0
	v_mov_b32_e32 v33, v74
	v_pk_add_f32 v[74:75], v[26:27], v[32:33]
	v_mul_f32_e32 v26, v15, v29
	v_pk_fma_f32 v[76:77], v[14:15], v[28:29], v[26:27] op_sel_hi:[1,1,0]
	v_mul_f32_e32 v26, v11, v31
	v_mov_b32_e32 v77, v80
	v_pk_fma_f32 v[80:81], v[10:11], v[30:31], v[26:27] op_sel_hi:[1,1,0]
	ds_read_b128 v[26:29], v128 offset:63488
	ds_read_b128 v[30:33], v128 offset:64512
	v_mov_b32_e32 v81, v82
	v_pk_add_f32 v[76:77], v[76:77], v[80:81]
	s_waitcnt lgkmcnt(0)
	v_mul_f32_e32 v30, v16, v30
	v_pk_add_f32 v[74:75], v[74:75], v[76:77]
	v_mov_b32_e32 v25, v30
	v_add_f32_e32 v74, v74, v75
	v_mul_f32_e32 v75, v17, v31
	v_pk_add_f32 v[30:31], v[118:119], v[118:119] op_sel:[0,1] op_sel_hi:[1,0]
	v_mul_f32_e32 v76, v12, v32
	v_mov_b32_e32 v31, v75
	v_pk_add_f32 v[30:31], v[24:25], v[30:31]
	v_mul_f32_e32 v24, v15, v27
	v_mul_f32_e32 v77, v13, v33
	v_pk_fma_f32 v[32:33], v[14:15], v[26:27], v[24:25] op_sel_hi:[1,1,0]
	v_mul_f32_e32 v24, v11, v29
	v_pk_fma_f32 v[28:29], v[10:11], v[28:29], v[24:25] op_sel_hi:[1,1,0]
	ds_read_b128 v[24:27], v137 offset:49152
	v_mov_b32_e32 v33, v76
	v_mov_b32_e32 v29, v77
	v_pk_add_f32 v[28:29], v[32:33], v[28:29]
	s_nop 0
	v_pk_add_f32 v[28:29], v[30:31], v[28:29]
	s_nop 0
	v_add_f32_e32 v32, v28, v29
	ds_read_b128 v[28:31], v137 offset:57344
	s_waitcnt lgkmcnt(1)
; #define LAS __attribute__((address_space(3)))
; __device__ __forceinline__ unsigned pk2(float lo, float hi) { return f2bf(lo) | (f2bf(hi) << 16); }
; template <bool ROUTER, bool OUT8, bool IN16>
; __device__ __forceinline__ void rms_rows(const Ctx& X, const void* __restrict__ Xin, void* __restrict__ Hv, const LAS float* sh, const LAS float* gs,
;                                          const LAS float* router_w_lds, unsigned* cnt, unsigned* route) {
;     ...
;         for (int j = 0; j < 8; ++j) { const int c = 4 * X.lane + 256 * j;
;             const f32x4 g4 = *(const LAS f32x4*)(gs + c), s4 = *(const LAS f32x4*)(sh + c);
;             const f32x4 h = v[j] * r * g4 + s4;
;             if (OUT8) { const unsigned q_ = pg8::pk4_fp8(h[0] * pg8::A8_SCALE, h[1] * pg8::A8_SCALE, h[2] * pg8::A8_SCALE, h[3] * pg8::A8_SCALE); if (ROUTER) hq[j] = q_; else *(unsigned*)((unsigned char*)Hv + (size_t)t * DM + c) = q_; }
;             else { v2u o; o.x = pk2(h[0], h[1]); o.y = pk2(h[2], h[3]); *(v2u*)((bf16*)Hv + (size_t)t * DM + c) = o; }
;             if (ROUTER) {
; #pragma unroll
;                 for (int e = 0; e < 8; ++e) { const f32x4 w = *(const LAS f32x4*)((const LAS float*)router_w_lds + e * DM + c);
;                     lg[e] += (h[0] * w[0] + h[1] * w[1]) + (h[2] * w[2] + h[3] * w[3]); } }
;         }
;         if (ROUTER) {
; #pragma unroll
;             for (int e = 0; e < 8; ++e) lg[e] = wave_sum(lg[e]);
	v_mul_f32_e32 v24, v16, v24
	v_mul_f32_e32 v33, v17, v25
	v_mov_b32_e32 v21, v24
	v_pk_add_f32 v[24:25], v[84:85], v[84:85] op_sel:[0,1] op_sel_hi:[1,0]
	v_mul_f32_e32 v26, v12, v26
	v_mov_b32_e32 v25, v33
	v_pk_add_f32 v[20:21], v[20:21], v[24:25]
	v_mul_f32_e32 v24, v15, v99
	v_pk_fma_f32 v[24:25], v[14:15], v[98:99], v[24:25] op_sel_hi:[1,1,0]
	v_mul_f32_e32 v75, v13, v27
	v_mov_b32_e32 v25, v26
	v_mul_f32_e32 v26, v11, v101
	v_pk_fma_f32 v[26:27], v[10:11], v[100:101], v[26:27] op_sel_hi:[1,1,0]
	s_nop 0
	v_mov_b32_e32 v27, v75
	v_pk_add_f32 v[24:25], v[24:25], v[26:27]
	s_waitcnt lgkmcnt(0)
	v_mul_f32_e32 v27, v16, v28
	v_pk_add_f32 v[20:21], v[20:21], v[24:25]
	v_mul_f32_e32 v28, v17, v29
	v_add_f32_e32 v26, v20, v21
	v_mov_b32_e32 v20, v96
	v_mov_b32_e32 v21, v86
	v_mov_b32_e32 v86, v97
	v_pk_add_f32 v[20:21], v[20:21], v[86:87]
	ds_bpermute_b32 v25, v78, v21
	ds_bpermute_b32 v24, v78, v20
	v_mov_b32_e32 v19, v27
	v_mov_b32_e32 v23, v28
	v_pk_add_f32 v[18:19], v[18:19], v[22:23]
	v_mul_f32_e32 v22, v15, v3
	s_waitcnt lgkmcnt(0)
	v_pk_add_f32 v[20:21], v[20:21], v[24:25]
	ds_bpermute_b32 v25, v138, v21
	ds_bpermute_b32 v24, v138, v20
	v_pk_fma_f32 v[2:3], v[14:15], v[2:3], v[22:23] op_sel_hi:[1,1,0]
	v_mul_f32_e32 v29, v12, v30
	v_mul_f32_e32 v30, v13, v31
	v_mov_b32_e32 v3, v29
	s_waitcnt lgkmcnt(0)
	v_pk_add_f32 v[20:21], v[20:21], v[24:25]
	ds_bpermute_b32 v23, v139, v21
	ds_bpermute_b32 v22, v139, v20
	v_mul_f32_e32 v24, v11, v5
	v_pk_fma_f32 v[4:5], v[10:11], v[4:5], v[24:25] op_sel_hi:[1,1,0]
	ds_bpermute_b32 v24, v78, v34
	v_mov_b32_e32 v5, v30
	s_waitcnt lgkmcnt(1)
	v_pk_add_f32 v[20:21], v[20:21], v[22:23]
	ds_bpermute_b32 v23, v140, v21
	ds_bpermute_b32 v22, v140, v20
	s_waitcnt lgkmcnt(2)
	v_add_f32_e32 v24, v34, v24
	v_pk_add_f32 v[2:3], v[2:3], v[4:5]
	ds_bpermute_b32 v25, v138, v24
	v_pk_add_f32 v[2:3], v[18:19], v[2:3]
	s_waitcnt lgkmcnt(1)
	v_pk_add_f32 v[4:5], v[20:21], v[22:23]
	ds_bpermute_b32 v21, v141, v5
	ds_bpermute_b32 v20, v141, v4
	s_waitcnt lgkmcnt(2)
	v_add_f32_e32 v22, v24, v25
	v_add_f32_e32 v18, v2, v3
	ds_bpermute_b32 v23, v139, v22
	ds_bpermute_b32 v19, v78, v79
	s_waitcnt lgkmcnt(2)
	v_pk_add_f32 v[2:3], v[4:5], v[20:21]
	ds_bpermute_b32 v20, v78, v74
	ds_bpermute_b32 v5, v142, v3
	s_waitcnt lgkmcnt(3)
	v_add_f32_e32 v4, v22, v23
	s_waitcnt lgkmcnt(2)
	v_add_f32_e32 v19, v79, v19
	ds_bpermute_b32 v21, v140, v4
	s_waitcnt lgkmcnt(2)
	v_add_f32_e32 v20, v74, v20
	ds_bpermute_b32 v23, v138, v20
	ds_bpermute_b32 v22, v138, v19
	s_waitcnt lgkmcnt(2)
	v_add_f32_e32 v21, v4, v21
	ds_bpermute_b32 v24, v141, v21
	s_waitcnt lgkmcnt(2)
	v_add_f32_e32 v20, v20, v23
	ds_bpermute_b32 v23, v139, v20
	s_waitcnt lgkmcnt(2)
	v_add_f32_e32 v19, v19, v22
	ds_bpermute_b32 v22, v139, v19
	ds_bpermute_b32 v4, v142, v2
	s_waitcnt lgkmcnt(3)
	v_add_f32_e32 v21, v21, v24
	s_waitcnt lgkmcnt(2)
	v_add_f32_e32 v20, v20, v23
	ds_bpermute_b32 v23, v140, v20
	s_waitcnt lgkmcnt(2)
	v_add_f32_e32 v19, v19, v22
	ds_bpermute_b32 v22, v140, v19
	ds_bpermute_b32 v24, v142, v21
	s_waitcnt lgkmcnt(3)
	v_pk_add_f32 v[4:5], v[2:3], v[4:5]
	s_waitcnt lgkmcnt(2)
	v_add_f32_e32 v2, v20, v23
	ds_bpermute_b32 v3, v141, v2
	s_waitcnt lgkmcnt(2)
	v_add_f32_e32 v19, v19, v22
	s_waitcnt lgkmcnt(1)
	v_add_f32_e32 v20, v21, v24
	ds_bpermute_b32 v24, v78, v18
	ds_bpermute_b32 v22, v141, v19
	s_waitcnt lgkmcnt(2)
	v_add_f32_e32 v2, v2, v3
	ds_bpermute_b32 v3, v78, v26
	ds_bpermute_b32 v23, v142, v2
	s_waitcnt lgkmcnt(3)
	v_add_f32_e32 v18, v18, v24
	s_waitcnt lgkmcnt(2)
	v_add_f32_e32 v19, v19, v22
	ds_bpermute_b32 v22, v78, v32
	s_waitcnt lgkmcnt(2)
	v_add_f32_e32 v3, v26, v3
	ds_bpermute_b32 v24, v138, v18
	ds_bpermute_b32 v26, v138, v3
	ds_bpermute_b32 v21, v142, v19
	s_waitcnt lgkmcnt(3)
	v_add_f32_e32 v22, v32, v22
	ds_bpermute_b32 v25, v138, v22
	s_waitcnt lgkmcnt(3)
	v_add_f32_e32 v18, v18, v24
	s_waitcnt lgkmcnt(2)
	v_add_f32_e32 v3, v3, v26
	ds_bpermute_b32 v24, v139, v18
	ds_bpermute_b32 v26, v139, v3
	s_waitcnt lgkmcnt(2)
	v_add_f32_e32 v22, v22, v25
	ds_bpermute_b32 v25, v139, v22
	v_cmp_gt_f32_e32 vcc, v4, v5
	s_waitcnt lgkmcnt(2)
	v_add_f32_e32 v18, v18, v24
	s_waitcnt lgkmcnt(1)
; template <bool ROUTER, bool OUT8, bool IN16>
; __device__ __forceinline__ void rms_rows(const Ctx& X, const void* __restrict__ Xin, void* __restrict__ Hv, const LAS float* sh, const LAS float* gs,
;                                          const LAS float* router_w_lds, unsigned* cnt, unsigned* route) {
;     ...
;             for (int e = 0; e < 8; ++e) lg[e] = wave_sum(lg[e]);
;             int e0 = 0; float m0 = lg[0];
; #pragma unroll
;             for (int e = 1; e < 8; ++e) if (lg[e] > m0) { m0 = lg[e]; e0 = e; }
;             int e1 = -1; float m1 = -INFINITY;
; #pragma unroll
;             for (int e = 0; e < 8; ++e) if (e != e0 && lg[e] > m1) { m1 = lg[e]; e1 = e; }
;             const float w0 = 1.0f / (1.0f + __expf(m1 - m0)), w1 = 1.0f - w0;
;             unsigned p0 = 0u, p1 = 0u;
;             if (X.lane == 0) {
;                 p0 = __hip_atomic_fetch_add(cnt + e0, 1u, RLX_AGENT); p1 = __hip_atomic_fetch_add(cnt + e1, 1u, RLX_AGENT);
;                 unsigned* rt = route + (size_t)t * 8;
;                 rt[0] = (unsigned)e0; rt[1] = (unsigned)e1; rt[2] = p0; rt[3] = p1; rt[4] = __float_as_uint(w0); rt[5] = __float_as_uint(w1); }
;             p0 = (unsigned)__builtin_amdgcn_readfirstlane((int)p0); p1 = (unsigned)__builtin_amdgcn_readfirstlane((int)p1);
;             unsigned char* d0 = (unsigned char*)Hv + ((size_t)e0 * NTOK + p0) * DM + 4 * X.lane; unsigned char* d1 = (unsigned char*)Hv + ((size_t)e1 * NTOK + p1) * DM + 4 * X.lane;
; #pragma unroll
;             for (int j = 0; j < 8; ++j) { *(unsigned*)(d0 + 256 * j) = hq[j]; *(unsigned*)(d1 + 256 * j) = hq[j]; }
	v_add_f32_e32 v3, v3, v26
	ds_bpermute_b32 v24, v140, v18
	ds_bpermute_b32 v26, v140, v3
	s_waitcnt lgkmcnt(2)
	v_add_f32_e32 v22, v22, v25
	ds_bpermute_b32 v25, v140, v22
	v_add_f32_e32 v19, v19, v21
	s_waitcnt lgkmcnt(2)
	v_add_f32_e32 v18, v18, v24
	s_waitcnt lgkmcnt(1)
	v_add_f32_e32 v3, v3, v26
	ds_bpermute_b32 v24, v141, v18
	ds_bpermute_b32 v26, v141, v3
	s_waitcnt lgkmcnt(2)
	v_add_f32_e32 v22, v22, v25
	ds_bpermute_b32 v25, v141, v22
	v_add_f32_e32 v21, v2, v23
	s_waitcnt lgkmcnt(2)
	v_add_f32_e32 v18, v18, v24
	s_waitcnt lgkmcnt(1)
	v_add_f32_e32 v3, v3, v26
	ds_bpermute_b32 v24, v142, v18
	ds_bpermute_b32 v26, v142, v3
	s_waitcnt lgkmcnt(2)
	v_add_f32_e32 v22, v22, v25
	ds_bpermute_b32 v25, v142, v22
	v_cmp_nlg_f32_e64 s[10:11], s29, v5
	s_waitcnt lgkmcnt(2)
	v_add_f32_e32 v2, v18, v24
	v_cndmask_b32_e32 v18, v5, v4, vcc
	s_waitcnt lgkmcnt(1)
	v_add_f32_e32 v23, v3, v26
	v_cndmask_b32_e64 v3, 0, 1, vcc
	v_cmp_gt_f32_e32 vcc, v20, v18
	s_waitcnt lgkmcnt(0)
	v_add_f32_e32 v22, v22, v25
	v_cndmask_b32_e32 v18, v18, v20, vcc
	v_cndmask_b32_e64 v3, v3, 2, vcc
	v_cmp_gt_f32_e32 vcc, v19, v18
	s_nop 1
	v_cndmask_b32_e32 v18, v18, v19, vcc
	v_cndmask_b32_e64 v3, v3, 3, vcc
	v_cmp_gt_f32_e32 vcc, v21, v18
	s_nop 1
	v_cndmask_b32_e32 v18, v18, v21, vcc
	v_cndmask_b32_e64 v3, v3, 4, vcc
	v_cmp_gt_f32_e32 vcc, v22, v18
	s_nop 1
	v_cndmask_b32_e32 v18, v18, v22, vcc
	v_cndmask_b32_e64 v3, v3, 5, vcc
	v_cmp_gt_f32_e64 s[6:7], v23, v18
	s_nop 1
	v_cndmask_b32_e64 v24, v3, 6, s[6:7]
	v_cndmask_b32_e64 v3, v18, v23, s[6:7]
	v_cmp_ngt_f32_e32 vcc, v2, v3
	s_nop 1
	v_cndmask_b32_e32 v34, 7, v24, vcc
	v_cmp_eq_u32_e64 s[8:9], 0, v34
	s_or_b64 s[8:9], s[8:9], s[10:11]
	s_nop 0
	v_cndmask_b32_e64 v5, v5, v126, s[8:9]
	v_cndmask_b32_e64 v18, 0, -1, s[8:9]
	v_cmp_ne_u32_e64 s[8:9], 1, v34
	v_cmp_gt_f32_e64 s[10:11], v4, v5
	s_and_b64 s[8:9], s[8:9], s[10:11]
	v_cndmask_b32_e64 v4, v5, v4, s[8:9]
	v_cndmask_b32_e64 v18, v18, 1, s[8:9]
	v_cmp_ne_u32_e64 s[8:9], 2, v34
	v_cmp_gt_f32_e64 s[10:11], v20, v4
	s_and_b64 s[8:9], s[8:9], s[10:11]
	v_cndmask_b32_e64 v4, v4, v20, s[8:9]
	v_cndmask_b32_e64 v5, v18, 2, s[8:9]
	v_cmp_ne_u32_e64 s[8:9], 3, v34
	v_cmp_gt_f32_e64 s[10:11], v19, v4
	s_and_b64 s[8:9], s[8:9], s[10:11]
	v_cndmask_b32_e64 v4, v4, v19, s[8:9]
	v_cndmask_b32_e64 v5, v5, 3, s[8:9]
	v_cmp_ne_u32_e64 s[8:9], 4, v34
	v_cmp_gt_f32_e64 s[10:11], v21, v4
	s_and_b64 s[8:9], s[8:9], s[10:11]
	v_cndmask_b32_e64 v4, v4, v21, s[8:9]
	v_cndmask_b32_e64 v5, v5, 4, s[8:9]
	v_cmp_ne_u32_e64 s[8:9], 5, v34
	v_cmp_gt_f32_e64 s[10:11], v22, v4
	s_and_b64 s[8:9], s[8:9], s[10:11]
	v_cndmask_b32_e64 v4, v4, v22, s[8:9]
	v_cndmask_b32_e64 v5, v5, 5, s[8:9]
	s_and_b64 s[8:9], s[6:7], vcc
	v_cmp_ngt_f32_e64 s[6:7], v23, v4
	s_or_b64 s[6:7], s[8:9], s[6:7]
	s_nop 0
	v_cndmask_b32_e64 v20, v23, v4, s[6:7]
	v_cndmask_b32_e64 v5, 6, v5, s[6:7]
	v_cmp_gt_f32_e64 s[6:7], v2, v20
	s_and_b64 s[6:7], vcc, s[6:7]
	s_nop 0
	v_cndmask_b32_e64 v18, v5, 7, s[6:7]
	v_ashrrev_i32_e32 v19, 31, v18
	s_and_saveexec_b64 s[8:9], s[4:5]
	s_xor_b64 s[8:9], exec, s[8:9]
	s_or_saveexec_b64 s[8:9], s[8:9]
	v_mov_b32_e32 v4, 0
	v_mov_b32_e32 v5, 0
	s_xor_b64 exec, exec, s[8:9]
	s_cbranch_execz .LBB0_3568
	v_mul_u32_u24_e32 v4, 0x1100, v34
	v_mul_u32_u24_e32 v22, 0x1100, v18
	v_add_u32_e32 v4, 0x10000, v4
	v_add_u32_e32 v22, 0x10000, v22
	global_atomic_add v4, v4, v125, s[88:89] sc0
	global_atomic_add v5, v22, v125, s[88:89] sc0
	v_cndmask_b32_e64 v20, v20, v2, s[6:7]
	v_cndmask_b32_e32 v2, v2, v3, vcc
	v_sub_f32_e32 v2, v20, v2
	v_mul_f32_e32 v2, 0x3fb8aa3b, v2
	v_exp_f32_e32 v3, v2
	v_mov_b32_e32 v2, v34
	v_add_f32_e32 v20, 1.0, v3
	v_div_scale_f32 v21, s[6:7], v20, v20, 1.0
	v_rcp_f32_e32 v22, v21
	v_div_scale_f32 v23, vcc, 1.0, v20, 1.0
	v_mov_b32_e32 v3, v18
	v_fma_f32 v24, -v21, v22, 1.0
	v_fmac_f32_e32 v22, v24, v22
	v_mul_f32_e32 v24, v23, v22
	v_fma_f32 v25, -v21, v24, v23
	v_fmac_f32_e32 v24, v25, v22
	v_fma_f32 v21, -v21, v24, v23
	v_div_fmas_f32 v21, v21, v22, v24
	v_div_fixup_f32 v20, v21, v20, 1.0
	v_sub_f32_e32 v21, 1.0, v20
	s_waitcnt vmcnt(0)
	global_store_dwordx4 v35, v[2:5], s[22:23]
	global_store_dwordx2 v35, v[20:21], s[22:23] offset:16
	s_branch .LBB0_3568

; #define LAS __attribute__((address_space(3)))
; #define REPS(P) for (int rep_ = 0; rep_ < ((P) == PROBE_REP ? 2 : 1); ++rep_)
; #define REPBAR() do { if (rep_) GRID_BAR(); } while (0)
; __device__ __forceinline__ void moe_tab(const Ctx& X, const unsigned* cnt, LAS int* tab) {
;     __syncthreads();
;     if (X.tid < 64) {
;         int n = X.tid < 8 ? (int)((__hip_atomic_load(cnt + (X.tid & 7), RLX_AGENT) + 255u) >> 8) : 0, inc = n;
; #pragma unroll
;         for (int o = 1; o < 8; o <<= 1) { const int v = __shfl_up(inc, o); if ((X.tid & 63) >= o) inc += v; }
;         if (X.tid < 8) tab[X.tid] = inc - n;
;         if (X.tid == 7) tab[8] = inc; }
; template <int l>
; __device__ __forceinline__ void layer_body(unsigned char* lds_raw, const Args& args, const XcdBarrier& bar, const int lo, const int hi) {
;     ...
;             if (IN(22)) REPS(22) { REPBAR(); const Ctx X = make_ctx(lds_raw);
;                 moe_tab(X, ctl + CW_CNT, tab);
.LBB0_3630:
	s_cmp_lt_i32 s40, 23
	s_cselect_b64 s[0:1], -1, 0
	s_cmp_gt_i32 s40, 22
	s_cselect_b64 s[4:5], -1, 0
	s_cmp_lt_i32 s41, 23
	s_cselect_b64 s[6:7], -1, 0
	s_or_b64 s[4:5], s[4:5], s[6:7]
	s_and_b64 vcc, exec, s[4:5]
	s_cbranch_vccnz .LBB0_3658
	v_mov_b32_e32 v1, v0
	s_load_dword s8, s[96:97], 0xf8
	v_cmp_gt_i32_e32 vcc, 64, v1
	s_waitcnt vmcnt(0) lgkmcnt(0)
	s_barrier
	s_and_saveexec_b64 s[6:7], vcc
	s_cbranch_execz .LBB0_3637
	v_cmp_gt_i32_e32 vcc, 8, v1
	v_mov_b32_e32 v2, 0
	s_and_saveexec_b64 s[4:5], vcc
	s_cbranch_execz .LBB0_3634
	v_and_b32_e32 v2, 7, v1
	v_mul_u32_u24_e32 v2, 0x1100, v2
	v_add_u32_e32 v2, 0x10000, v2
	global_load_dword v2, v2, s[88:89] sc1
	s_waitcnt vmcnt(0)
	v_add_u32_e32 v2, 0xff, v2
	v_lshrrev_b32_e32 v2, 8, v2

; #define LAS __attribute__((address_space(3)))
; #define REPS(P) for (int rep_ = 0; rep_ < ((P) == PROBE_REP ? 2 : 1); ++rep_)
; #define REPBAR() do { if (rep_) GRID_BAR(); } while (0)
; __device__ __forceinline__ void moe_tab(const Ctx& X, const unsigned* cnt, LAS int* tab) {
;     __syncthreads();
;     if (X.tid < 64) {
;         int n = X.tid < 8 ? (int)((__hip_atomic_load(cnt + (X.tid & 7), RLX_AGENT) + 255u) >> 8) : 0, inc = n;
; #pragma unroll
;         for (int o = 1; o < 8; o <<= 1) { const int v = __shfl_up(inc, o); if ((X.tid & 63) >= o) inc += v; }
;         if (X.tid < 8) tab[X.tid] = inc - n;
;         if (X.tid == 7) tab[8] = inc; }
; template <int l>
; __device__ __forceinline__ void layer_body(unsigned char* lds_raw, const Args& args, const XcdBarrier& bar, const int lo, const int hi) {
;     ...
;             if (IN(23)) REPS(23) { REPBAR(); const Ctx X = make_ctx(lds_raw);
;                 moe_tab(X, ctl + CW_CNT, tab);
.LBB0_3712:
	s_cmp_lt_i32 s40, 24
	s_cselect_b64 s[0:1], -1, 0
	s_add_u32 s8, s88, 0x59600000
	s_addc_u32 s9, s89, 0
	s_and_b64 s[4:5], s[0:1], s[4:5]
	s_andn2_b64 vcc, exec, s[4:5]
	s_cbranch_vccnz .LBB0_3769
	v_mov_b32_e32 v172, v0
	v_lshrrev_b32_e32 v1, 5, v0
	s_waitcnt vmcnt(0)
	v_bfe_u32 v2, v0, 2, 2
	s_load_dword s60, s[96:97], 0xf8
	v_and_or_b32 v1, v1, 4, v2
	v_lshrrev_b32_e32 v2, 3, v0
	v_lshrrev_b32_e32 v4, 1, v0
	v_and_b32_e32 v3, 32, v2
	v_and_b32_e32 v4, 24, v4
	v_or3_b32 v1, v1, v3, v4
	v_bfe_u32 v3, v0, 2, 4
	v_and_or_b32 v2, v2, 48, v3
	v_cmp_gt_i32_e32 vcc, 64, v172
	s_waitcnt lgkmcnt(0)
	s_barrier
	s_and_saveexec_b64 s[6:7], vcc
	s_cbranch_execz .LBB0_3719
	v_cmp_gt_i32_e32 vcc, 8, v172
	v_mov_b32_e32 v3, 0
	s_and_saveexec_b64 s[4:5], vcc
	s_cbranch_execz .LBB0_3716
	v_and_b32_e32 v3, 7, v172
	v_mul_u32_u24_e32 v3, 0x1100, v3
	v_add_u32_e32 v3, 0x10000, v3
	global_load_dword v3, v3, s[88:89] sc1
	s_waitcnt vmcnt(0)
	v_add_u32_e32 v3, 0xff, v3
	v_lshrrev_b32_e32 v3, 8, v3

; #define LAS __attribute__((address_space(3)))
; #define REPS(P) for (int rep_ = 0; rep_ < ((P) == PROBE_REP ? 2 : 1); ++rep_)
; #define REPBAR() do { if (rep_) GRID_BAR(); } while (0)
; __device__ __forceinline__ void moe_tab(const Ctx& X, const unsigned* cnt, LAS int* tab) {
;     __syncthreads();
;     if (X.tid < 64) {
;         int n = X.tid < 8 ? (int)((__hip_atomic_load(cnt + (X.tid & 7), RLX_AGENT) + 255u) >> 8) : 0, inc = n;
; #pragma unroll
;         for (int o = 1; o < 8; o <<= 1) { const int v = __shfl_up(inc, o); if ((X.tid & 63) >= o) inc += v; }
;         if (X.tid < 8) tab[X.tid] = inc - n;
;         if (X.tid == 7) tab[8] = inc; }
; template <int l>
; __device__ __forceinline__ void layer_body(unsigned char* lds_raw, const Args& args, const XcdBarrier& bar, const int lo, const int hi) {
;     ...
;             if (IN(24)) REPS(24) { REPBAR(); const Ctx X = make_ctx(lds_raw); moe_tab(X, ctl + CW_CNT, tab); moe_combine_final(X, XA, YG, (const bf16*)(ws + WS_YG2), 2 * X.G, ROUTE, tab, modl + 5 * DM, (const float*)args.in[26], args.out); }
.LBB0_3823:
	s_cmp_gt_i32 s40, 24
	s_cselect_b64 s[0:1], -1, 0
	s_xor_b64 s[4:5], s[4:5], -1
	s_or_b64 s[0:1], s[0:1], s[4:5]
	s_and_b64 vcc, exec, s[0:1]
	s_cbranch_vccnz .LBB0_3870
	s_load_dword s3, s[96:97], 0xf8
	s_waitcnt vmcnt(0)
	v_and_b32_e32 v72, 63, v0
	v_readfirstlane_b32 s6, v0
	v_cmp_gt_i32_e32 vcc, 64, v0
	s_waitcnt lgkmcnt(0)
	s_barrier
	s_and_saveexec_b64 s[4:5], vcc
	s_cbranch_execz .LBB0_3830
	v_cmp_gt_i32_e32 vcc, 8, v0
	v_mov_b32_e32 v1, 0
	s_and_saveexec_b64 s[0:1], vcc
	s_cbranch_execz .LBB0_3827
	v_and_b32_e32 v1, 7, v0
	v_mul_u32_u24_e32 v1, 0x1100, v1
	v_add_u32_e32 v1, 0x10000, v1
	global_load_dword v1, v1, s[88:89] sc1
	s_waitcnt vmcnt(0)
	v_add_u32_e32 v1, 0xff, v1
	v_lshrrev_b32_e32 v1, 8, v1
